# fp8 GEMMs: MX-scaled MFMA with unit scales replaced by the plain v_mfma_f32_16x16x128_f8f6f4 (same fp8 e4m3 operands, same f32 accumulate, scale was exactly 1.0); plus the NSA mask change
# speedup vs baseline: 1.0323x; 1.0236x over previous
.LBB0_982:
	v_add_u32_e32 v129, s31, v128
	v_ashrrev_i32_e32 v131, 3, v129
	v_lshlrev_b32_e32 v130, 4, v128
	v_lshlrev_b32_e32 v136, 1, v131
	v_lshrrev_b32_e32 v137, 2, v131
	v_bitop3_b32 v130, v129, s55, v130 bitop3:0x48
	v_and_b32_e32 v136, 24, v136
	v_and_b32_e32 v137, 4, v137
	v_and_b32_e32 v138, 0x1fffe3, v131
	v_lshl_add_u32 v129, v129, 4, v132
	v_or3_b32 v136, v138, v137, v136
	v_ashrrev_i32_e32 v129, 7, v129
	v_lshl_or_b32 v244, v136, 11, v130
	v_lshlrev_b32_e32 v136, 1, v129
	v_lshrrev_b32_e32 v137, 2, v129
	v_and_b32_e32 v136, 24, v136
	v_and_b32_e32 v137, 4, v137
	v_and_b32_e32 v138, 0x1fffe3, v129
	v_or3_b32 v136, v138, v137, v136
	v_lshl_or_b32 v245, v136, 11, v130
	v_and_b32_e32 v136, 15, v128
	v_lshrrev_b32_e32 v137, 3, v128
	v_bfe_u32 v128, v128, 1, 3
	s_mov_b32 s10, 0xffffffe
	v_lshlrev_b32_e32 v136, 7, v136
	v_and_b32_e32 v138, 0xffffffe, v137
	v_bitop3_b32 v137, v137, v128, s10 bitop3:0x6c
	v_or_b32_e32 v168, s70, v136
	v_or_b32_e32 v136, s71, v136
	v_lshlrev_b32_e32 v169, 4, v137
	v_bitop3_b32 v128, v138, v128, 1 bitop3:0x36
	v_add_u32_e32 v246, v169, v136
	v_lshlrev_b32_e32 v128, 4, v128
	v_add_u32_e32 v247, v128, v136
	v_lshl_or_b32 v249, v129, 11, v130
	v_add_u32_e32 v129, s85, v246
	v_lshl_or_b32 v248, v131, 11, v130
	v_add_u32_e32 v130, s85, v247
	ds_read_b128 v[136:139], v129
	ds_read_b128 v[144:147], v129 offset:2048
	ds_read_b128 v[140:143], v130
	ds_read_b128 v[148:151], v130 offset:2048
	v_add_u32_e32 v129, s86, v246
	v_add_u32_e32 v130, s86, v247
	ds_read_b128 v[152:155], v129
	ds_read_b128 v[160:163], v129 offset:2048
	ds_read_b128 v[156:159], v130
	ds_read_b128 v[164:167], v130 offset:2048
	s_add_i32 s10, s97, 0xffffff80
	s_add_i32 s11, s10, s94
	s_cmpk_eq_i32 s97, 0x880
	s_cselect_b32 s40, s37, s91
	s_cselect_b32 s10, 0, s10
	s_cselect_b32 s39, 0x80, s97
	s_cselect_b32 s38, s36, s11
	s_add_i32 s11, s91, s97
	v_add_u32_e32 v250, 0x40000, v248
	v_add_u32_e32 v251, 0x40000, v249
	s_add_i32 s39, s40, s39
	s_addk_i32 s11, 0xff00
	s_add_i32 s40, s40, s10
	v_add3_u32 v252, v169, v168, 0
	s_mov_b32 m0, s72
	v_add3_u32 v253, v128, v168, 0
	ds_read_b128 v[168:171], v252
	ds_read_b128 v[176:179], v252 offset:2048
	ds_read_b128 v[172:175], v253
	ds_read_b128 v[180:183], v253 offset:2048
	ds_read_b128 v[184:187], v252 offset:4096
	ds_read_b128 v[192:195], v252 offset:6144
	ds_read_b128 v[188:191], v253 offset:4096
	ds_read_b128 v[196:199], v253 offset:6144
	buffer_load_dwordx4 v250, s[12:15], s11 offen lds
	s_mov_b32 m0, s75
	s_nop 0
	buffer_load_dwordx4 v251, s[12:15], s11 offen lds
	s_waitcnt vmcnt(8)
	s_waitcnt lgkmcnt(0)
	s_barrier
	s_setprio 1
	s_waitcnt lgkmcnt(5)
	v_mfma_f32_16x16x128_f8f6f4 v[124:127], v[136:143], v[168:175], v[124:127]
	v_mfma_f32_16x16x128_f8f6f4 v[120:123], v[144:151], v[168:175], v[120:123]
	s_waitcnt lgkmcnt(4)
	v_mfma_f32_16x16x128_f8f6f4 v[112:115], v[136:143], v[176:183], v[112:115]
	v_mfma_f32_16x16x128_f8f6f4 v[104:107], v[144:151], v[176:183], v[104:107]
	s_waitcnt lgkmcnt(1)
	v_mfma_f32_16x16x128_f8f6f4 v[96:99], v[136:143], v[184:191], v[96:99]
	v_mfma_f32_16x16x128_f8f6f4 v[128:131], v[144:151], v[184:191], v[88:91]
	s_waitcnt lgkmcnt(0)
	v_mfma_f32_16x16x128_f8f6f4 v[200:203], v[136:143], v[192:199], v[80:83]
	v_mfma_f32_16x16x128_f8f6f4 v[204:207], v[144:151], v[192:199], v[72:75]
	s_setprio 0
	s_setprio 1
	v_mfma_f32_16x16x128_f8f6f4 v[116:119], v[152:159], v[168:175], v[116:119]
	v_mfma_f32_16x16x128_f8f6f4 v[108:111], v[160:167], v[168:175], v[108:111]
	v_mfma_f32_16x16x128_f8f6f4 v[100:103], v[152:159], v[176:183], v[100:103]
	v_mfma_f32_16x16x128_f8f6f4 v[168:171], v[160:167], v[176:183], v[92:95]
	v_mfma_f32_16x16x128_f8f6f4 v[172:175], v[152:159], v[184:191], v[84:87]
	v_mfma_f32_16x16x128_f8f6f4 v[176:179], v[160:167], v[184:191], v[76:79]
	v_mfma_f32_16x16x128_f8f6f4 v[180:183], v[152:159], v[192:199], v[68:71]
	v_mfma_f32_16x16x128_f8f6f4 v[184:187], v[160:167], v[192:199], v[64:67]
	s_setprio 0
	s_barrier
	s_mov_b32 m0, s57
	s_mov_b32 s10, s14
	s_mov_b32 s11, s15
	s_nop 1
	ds_read_b128 v[64:67], v252 offset:16384
	ds_read_b128 v[72:75], v252 offset:18432
	ds_read_b128 v[68:71], v253 offset:16384
	ds_read_b128 v[76:79], v253 offset:18432
	ds_read_b128 v[80:83], v252 offset:20480
	ds_read_b128 v[88:91], v252 offset:22528
	ds_read_b128 v[84:87], v253 offset:20480
	ds_read_b128 v[92:95], v253 offset:22528
	buffer_load_dwordx4 v244, s[8:11], s38 offen lds
	s_mov_b32 m0, s58
	s_add_i32 s41, s38, 0x40000
	buffer_load_dwordx4 v245, s[8:11], s38 offen lds
	s_mov_b32 m0, s59
	s_nop 0
	buffer_load_dwordx4 v244, s[8:11], s41 offen lds
	s_mov_b32 m0, s60
	s_nop 0
	buffer_load_dwordx4 v245, s[8:11], s41 offen lds
	s_mov_b32 m0, s56
	s_nop 0
	buffer_load_dwordx4 v248, s[12:15], s40 offen lds
	s_mov_b32 m0, s61
	s_nop 0
	buffer_load_dwordx4 v249, s[12:15], s40 offen lds
	s_waitcnt vmcnt(8)
	s_waitcnt lgkmcnt(0)
	s_barrier
	s_setprio 1
	s_waitcnt lgkmcnt(5)
	v_mfma_f32_16x16x128_f8f6f4 v[60:63], v[136:143], v[64:71], v[60:63]
	v_mfma_f32_16x16x128_f8f6f4 v[56:59], v[144:151], v[64:71], v[56:59]
	s_waitcnt lgkmcnt(4)
	v_mfma_f32_16x16x128_f8f6f4 v[48:51], v[136:143], v[72:79], v[48:51]
	v_mfma_f32_16x16x128_f8f6f4 v[188:191], v[144:151], v[72:79], v[40:43]
	s_waitcnt lgkmcnt(1)
	v_mfma_f32_16x16x128_f8f6f4 v[192:195], v[136:143], v[80:87], v[32:35]
	v_mfma_f32_16x16x128_f8f6f4 v[196:199], v[144:151], v[80:87], v[24:27]
	s_waitcnt lgkmcnt(0)
	v_mfma_f32_16x16x128_f8f6f4 v[208:211], v[136:143], v[88:95], v[16:19]
	v_mfma_f32_16x16x128_f8f6f4 v[212:215], v[144:151], v[88:95], v[8:11]
	s_setprio 0
	s_setprio 1
	v_mfma_f32_16x16x128_f8f6f4 v[52:55], v[152:159], v[64:71], v[52:55]
	v_mfma_f32_16x16x128_f8f6f4 v[216:219], v[160:167], v[64:71], v[44:47]
	v_mfma_f32_16x16x128_f8f6f4 v[220:223], v[152:159], v[72:79], v[36:39]
	v_mfma_f32_16x16x128_f8f6f4 v[224:227], v[160:167], v[72:79], v[28:31]
	v_mfma_f32_16x16x128_f8f6f4 v[228:231], v[152:159], v[80:87], v[20:23]
	v_mfma_f32_16x16x128_f8f6f4 v[232:235], v[160:167], v[80:87], v[12:15]
	v_mfma_f32_16x16x128_f8f6f4 v[236:239], v[152:159], v[88:95], v[4:7]
	v_mfma_f32_16x16x128_f8f6f4 v[240:243], v[160:167], v[88:95], v[0:3]
	s_setprio 0
	s_barrier
	s_add_i32 s41, 0, 0x18000
	s_nop 2
	v_add_u32_e32 v4, s41, v246
	v_add_u32_e32 v12, s41, v247
	s_add_i32 s41, 0, 0x1c000
	v_add_u32_e32 v16, s41, v246
	ds_read_b128 v[0:3], v4
	ds_read_b128 v[8:11], v4 offset:2048
	ds_read_b128 v[4:7], v12
	ds_read_b128 v[12:15], v12 offset:2048
	v_add_u32_e32 v17, s41, v247
	ds_read_b128 v[136:139], v16
	ds_read_b128 v[144:147], v16 offset:2048
	ds_read_b128 v[140:143], v17
	ds_read_b128 v[148:151], v17 offset:2048
	s_mov_b32 m0, s62
	ds_read_b128 v[16:19], v252 offset:32768
	ds_read_b128 v[24:27], v252 offset:34816
	ds_read_b128 v[20:23], v253 offset:32768
	ds_read_b128 v[28:31], v253 offset:34816
	ds_read_b128 v[32:35], v252 offset:36864
	ds_read_b128 v[40:43], v252 offset:38912
	ds_read_b128 v[36:39], v253 offset:36864
	ds_read_b128 v[44:47], v253 offset:38912
	buffer_load_dwordx4 v250, s[12:15], s40 offen lds
	s_mov_b32 m0, s63
	s_nop 0
	buffer_load_dwordx4 v251, s[12:15], s40 offen lds
	s_waitcnt vmcnt(8)
	s_waitcnt lgkmcnt(0)
	s_barrier
	s_setprio 1
	s_waitcnt lgkmcnt(5)
	v_mfma_f32_16x16x128_f8f6f4 v[124:127], v[0:7], v[16:23], v[124:127]
	v_mfma_f32_16x16x128_f8f6f4 v[120:123], v[8:15], v[16:23], v[120:123]
	s_waitcnt lgkmcnt(4)
	v_mfma_f32_16x16x128_f8f6f4 v[112:115], v[0:7], v[24:31], v[112:115]
	v_mfma_f32_16x16x128_f8f6f4 v[104:107], v[8:15], v[24:31], v[104:107]
	s_waitcnt lgkmcnt(1)
	v_mfma_f32_16x16x128_f8f6f4 v[96:99], v[0:7], v[32:39], v[96:99]
	v_mfma_f32_16x16x128_f8f6f4 v[88:91], v[8:15], v[32:39], v[128:131]
	s_waitcnt lgkmcnt(0)
	v_mfma_f32_16x16x128_f8f6f4 v[80:83], v[0:7], v[40:47], v[200:203]
	v_mfma_f32_16x16x128_f8f6f4 v[72:75], v[8:15], v[40:47], v[204:207]
	s_setprio 0
	s_setprio 1
	v_mfma_f32_16x16x128_f8f6f4 v[116:119], v[136:143], v[16:23], v[116:119]
	v_mfma_f32_16x16x128_f8f6f4 v[108:111], v[144:151], v[16:23], v[108:111]
	v_mfma_f32_16x16x128_f8f6f4 v[100:103], v[136:143], v[24:31], v[100:103]
	v_mfma_f32_16x16x128_f8f6f4 v[92:95], v[144:151], v[24:31], v[168:171]
	v_mfma_f32_16x16x128_f8f6f4 v[84:87], v[136:143], v[32:39], v[172:175]
	v_mfma_f32_16x16x128_f8f6f4 v[76:79], v[144:151], v[32:39], v[176:179]
	v_mfma_f32_16x16x128_f8f6f4 v[68:71], v[136:143], v[40:47], v[180:183]
	v_mfma_f32_16x16x128_f8f6f4 v[64:67], v[144:151], v[40:47], v[184:187]
	s_setprio 0
	s_barrier
	s_mov_b32 m0, s64
	s_add_i32 s40, s38, 0x80
	ds_read_b128 v[152:155], v252 offset:49152
	ds_read_b128 v[160:163], v252 offset:51200
	ds_read_b128 v[156:159], v253 offset:49152
	ds_read_b128 v[164:167], v253 offset:51200
	ds_read_b128 v[168:171], v252 offset:53248
	ds_read_b128 v[176:179], v252 offset:55296
	ds_read_b128 v[172:175], v253 offset:53248
	ds_read_b128 v[180:183], v253 offset:55296
	buffer_load_dwordx4 v244, s[8:11], s40 offen lds
	s_mov_b32 m0, s65
	s_add_i32 s38, s38, 0x40080
	buffer_load_dwordx4 v245, s[8:11], s40 offen lds
	s_mov_b32 m0, s68
	s_nop 0
	buffer_load_dwordx4 v244, s[8:11], s38 offen lds
	s_mov_b32 m0, s69
	s_nop 0
	buffer_load_dwordx4 v245, s[8:11], s38 offen lds
	s_mov_b32 m0, s66
	s_nop 0
	buffer_load_dwordx4 v248, s[12:15], s39 offen lds
	s_mov_b32 m0, s67
	s_nop 0
	buffer_load_dwordx4 v249, s[12:15], s39 offen lds
	s_waitcnt vmcnt(8)
	s_waitcnt lgkmcnt(0)
	s_barrier
	s_setprio 1
	s_waitcnt lgkmcnt(5)
	v_mfma_f32_16x16x128_f8f6f4 v[60:63], v[0:7], v[152:159], v[60:63]
	v_mfma_f32_16x16x128_f8f6f4 v[56:59], v[8:15], v[152:159], v[56:59]
	s_waitcnt lgkmcnt(4)
	v_mfma_f32_16x16x128_f8f6f4 v[48:51], v[0:7], v[160:167], v[48:51]
	v_mfma_f32_16x16x128_f8f6f4 v[40:43], v[8:15], v[160:167], v[188:191]
	s_waitcnt lgkmcnt(1)
	v_mfma_f32_16x16x128_f8f6f4 v[32:35], v[0:7], v[168:175], v[192:195]
	v_mfma_f32_16x16x128_f8f6f4 v[24:27], v[8:15], v[168:175], v[196:199]
	s_waitcnt lgkmcnt(0)
	v_mfma_f32_16x16x128_f8f6f4 v[16:19], v[0:7], v[176:183], v[208:211]
	v_mfma_f32_16x16x128_f8f6f4 v[8:11], v[8:15], v[176:183], v[212:215]
	s_setprio 0
	s_setprio 1
	v_mfma_f32_16x16x128_f8f6f4 v[52:55], v[136:143], v[152:159], v[52:55]
	v_mfma_f32_16x16x128_f8f6f4 v[44:47], v[144:151], v[152:159], v[216:219]
	v_mfma_f32_16x16x128_f8f6f4 v[36:39], v[136:143], v[160:167], v[220:223]
	v_mfma_f32_16x16x128_f8f6f4 v[28:31], v[144:151], v[160:167], v[224:227]
	v_mfma_f32_16x16x128_f8f6f4 v[20:23], v[136:143], v[168:175], v[228:231]
	v_mfma_f32_16x16x128_f8f6f4 v[12:15], v[144:151], v[168:175], v[232:235]
	v_mfma_f32_16x16x128_f8f6f4 v[4:7], v[136:143], v[176:183], v[236:239]
	v_mfma_f32_16x16x128_f8f6f4 v[0:3], v[144:151], v[176:183], v[240:243]
	s_setprio 0
	s_barrier
	s_add_i32 s96, s96, 2
	s_addk_i32 s97, 0x100
	s_cmp_gt_u32 s96, 13
	s_cbranch_scc1 .LBB0_1022

.LBB0_2173:
	v_add_u32_e32 v129, s17, v128
	v_lshlrev_b32_e32 v130, 4, v128
	v_ashrrev_i32_e32 v131, 3, v129
	v_bitop3_b32 v130, v129, s22, v130 bitop3:0x48
	v_lshlrev_b32_e32 v132, 1, v131
	v_lshrrev_b32_e32 v133, 2, v131
	v_lshl_add_u32 v129, v129, 4, v134
	v_and_b32_e32 v132, 24, v132
	v_and_b32_e32 v133, 4, v133
	v_and_b32_e32 v136, 0x1fffe3, v131
	v_ashrrev_i32_e32 v129, 7, v129
	v_or3_b32 v132, v136, v133, v132
	v_lshlrev_b32_e32 v133, 1, v129
	v_lshrrev_b32_e32 v136, 2, v129
	v_and_b32_e32 v133, 24, v133
	v_and_b32_e32 v136, 4, v136
	v_and_b32_e32 v137, 0x1fffe3, v129
	v_or3_b32 v133, v137, v136, v133
	v_and_b32_e32 v136, 15, v128
	v_lshrrev_b32_e32 v137, 3, v128
	v_bfe_u32 v128, v128, 1, 3
	v_lshlrev_b32_e32 v136, 7, v136
	v_and_b32_e32 v138, 0xffffffe, v137
	v_bitop3_b32 v137, v137, v128, s48 bitop3:0x6c
	v_or_b32_e32 v168, s42, v136
	v_or_b32_e32 v136, s43, v136
	v_lshlrev_b32_e32 v169, 4, v137
	v_bitop3_b32 v128, v138, v128, 1 bitop3:0x36
	v_add_u32_e32 v244, v169, v136
	v_lshlrev_b32_e32 v128, 4, v128
	v_add_u32_e32 v245, v128, v136
	v_lshl_or_b32 v247, v129, 11, v130
	v_add_u32_e32 v129, s49, v244
	v_lshl_or_b32 v132, v132, 11, v130
	v_lshl_or_b32 v133, v133, 11, v130
	v_lshl_or_b32 v246, v131, 11, v130
	v_add_u32_e32 v130, s49, v245
	ds_read_b128 v[136:139], v129
	ds_read_b128 v[144:147], v129 offset:2048
	ds_read_b128 v[140:143], v130
	ds_read_b128 v[148:151], v130 offset:2048
	v_add_u32_e32 v129, s50, v244
	v_add_u32_e32 v130, s50, v245
	ds_read_b128 v[152:155], v129
	ds_read_b128 v[160:163], v129 offset:2048
	ds_read_b128 v[156:159], v130
	ds_read_b128 v[164:167], v130 offset:2048
	s_add_i32 s6, s62, 0xffffff80
	s_add_i32 s7, s6, s57
	s_cmpk_eq_i32 s62, 0x880
	s_cselect_b32 s65, s35, s54
	s_cselect_b32 s6, 0, s6
	s_cselect_b32 s64, 0x80, s62
	s_cselect_b32 s63, s29, s7
	s_add_i32 s7, s54, s62
	v_add_u32_e32 v248, 0x40000, v246
	v_add_u32_e32 v249, 0x40000, v247
	s_add_i32 s64, s65, s64
	s_addk_i32 s7, 0xff00
	s_add_i32 s65, s65, s6
	v_add3_u32 v250, v169, v168, 0
	s_mov_b32 m0, s44
	v_add3_u32 v251, v128, v168, 0
	ds_read_b128 v[168:171], v250
	ds_read_b128 v[176:179], v250 offset:2048
	ds_read_b128 v[172:175], v251
	ds_read_b128 v[180:183], v251 offset:2048
	ds_read_b128 v[184:187], v250 offset:4096
	ds_read_b128 v[192:195], v250 offset:6144
	ds_read_b128 v[188:191], v251 offset:4096
	ds_read_b128 v[196:199], v251 offset:6144
	buffer_load_dwordx4 v248, s[8:11], s7 offen lds
	s_mov_b32 m0, s47
	s_nop 0
	buffer_load_dwordx4 v249, s[8:11], s7 offen lds
	s_waitcnt vmcnt(8)
	s_waitcnt lgkmcnt(0)
	s_barrier
	s_setprio 1
	s_waitcnt lgkmcnt(5)
	v_mfma_f32_16x16x128_f8f6f4 v[124:127], v[136:143], v[168:175], v[124:127]
	v_mfma_f32_16x16x128_f8f6f4 v[120:123], v[144:151], v[168:175], v[120:123]
	s_waitcnt lgkmcnt(4)
	v_mfma_f32_16x16x128_f8f6f4 v[108:111], v[136:143], v[176:183], v[108:111]
	v_mfma_f32_16x16x128_f8f6f4 v[104:107], v[144:151], v[176:183], v[104:107]
	s_waitcnt lgkmcnt(1)
	v_mfma_f32_16x16x128_f8f6f4 v[128:131], v[136:143], v[184:191], v[92:95]
	v_mfma_f32_16x16x128_f8f6f4 v[200:203], v[144:151], v[184:191], v[88:91]
	s_waitcnt lgkmcnt(0)
	v_mfma_f32_16x16x128_f8f6f4 v[204:207], v[136:143], v[192:199], v[76:79]
	v_mfma_f32_16x16x128_f8f6f4 v[208:211], v[144:151], v[192:199], v[72:75]
	s_setprio 0
	s_setprio 1
	v_mfma_f32_16x16x128_f8f6f4 v[116:119], v[152:159], v[168:175], v[116:119]
	v_mfma_f32_16x16x128_f8f6f4 v[112:115], v[160:167], v[168:175], v[112:115]
	v_mfma_f32_16x16x128_f8f6f4 v[100:103], v[152:159], v[176:183], v[100:103]
	v_mfma_f32_16x16x128_f8f6f4 v[96:99], v[160:167], v[176:183], v[96:99]
	v_mfma_f32_16x16x128_f8f6f4 v[168:171], v[152:159], v[184:191], v[84:87]
	v_mfma_f32_16x16x128_f8f6f4 v[172:175], v[160:167], v[184:191], v[80:83]
	v_mfma_f32_16x16x128_f8f6f4 v[176:179], v[152:159], v[192:199], v[68:71]
	v_mfma_f32_16x16x128_f8f6f4 v[180:183], v[160:167], v[192:199], v[64:67]
	s_setprio 0
	s_barrier
	s_mov_b32 m0, s26
	s_mov_b32 s6, s10
	s_mov_b32 s7, s11
	s_nop 1
	ds_read_b128 v[64:67], v250 offset:16384
	ds_read_b128 v[72:75], v250 offset:18432
	ds_read_b128 v[68:71], v251 offset:16384
	ds_read_b128 v[76:79], v251 offset:18432
	ds_read_b128 v[80:83], v250 offset:20480
	ds_read_b128 v[88:91], v250 offset:22528
	ds_read_b128 v[84:87], v251 offset:20480
	ds_read_b128 v[92:95], v251 offset:22528
	buffer_load_dwordx4 v132, s[4:7], s63 offen lds
	s_mov_b32 m0, s27
	s_add_i32 s66, s63, 0x40000
	buffer_load_dwordx4 v133, s[4:7], s63 offen lds
	s_mov_b32 m0, s28
	s_nop 0
	buffer_load_dwordx4 v132, s[4:7], s66 offen lds
	s_mov_b32 m0, s30
	s_nop 0
	buffer_load_dwordx4 v133, s[4:7], s66 offen lds
	s_mov_b32 m0, s25
	s_nop 0
	buffer_load_dwordx4 v246, s[8:11], s65 offen lds
	s_mov_b32 m0, s31
	s_nop 0
	buffer_load_dwordx4 v247, s[8:11], s65 offen lds
	s_waitcnt vmcnt(8)
	s_waitcnt lgkmcnt(0)
	s_barrier
	s_setprio 1
	s_waitcnt lgkmcnt(5)
	v_mfma_f32_16x16x128_f8f6f4 v[60:63], v[136:143], v[64:71], v[60:63]
	v_mfma_f32_16x16x128_f8f6f4 v[56:59], v[144:151], v[64:71], v[56:59]
	s_waitcnt lgkmcnt(4)
	v_mfma_f32_16x16x128_f8f6f4 v[184:187], v[136:143], v[72:79], v[44:47]
	v_mfma_f32_16x16x128_f8f6f4 v[188:191], v[144:151], v[72:79], v[40:43]
	s_waitcnt lgkmcnt(1)
	v_mfma_f32_16x16x128_f8f6f4 v[192:195], v[136:143], v[80:87], v[28:31]
	v_mfma_f32_16x16x128_f8f6f4 v[196:199], v[144:151], v[80:87], v[24:27]
	s_waitcnt lgkmcnt(0)
	v_mfma_f32_16x16x128_f8f6f4 v[212:215], v[136:143], v[88:95], v[12:15]
	v_mfma_f32_16x16x128_f8f6f4 v[216:219], v[144:151], v[88:95], v[8:11]
	s_setprio 0
	s_setprio 1
	v_mfma_f32_16x16x128_f8f6f4 v[52:55], v[152:159], v[64:71], v[52:55]
	v_mfma_f32_16x16x128_f8f6f4 v[48:51], v[160:167], v[64:71], v[48:51]
	v_mfma_f32_16x16x128_f8f6f4 v[220:223], v[152:159], v[72:79], v[36:39]
	v_mfma_f32_16x16x128_f8f6f4 v[224:227], v[160:167], v[72:79], v[32:35]
	v_mfma_f32_16x16x128_f8f6f4 v[228:231], v[152:159], v[80:87], v[20:23]
	v_mfma_f32_16x16x128_f8f6f4 v[232:235], v[160:167], v[80:87], v[16:19]
	v_mfma_f32_16x16x128_f8f6f4 v[236:239], v[152:159], v[88:95], v[4:7]
	v_mfma_f32_16x16x128_f8f6f4 v[240:243], v[160:167], v[88:95], v[0:3]
	s_setprio 0
	s_barrier
	s_add_i32 s66, 0, 0x18000
	s_nop 2
	v_add_u32_e32 v4, s66, v244
	v_add_u32_e32 v8, s66, v245
	s_add_i32 s66, 0, 0x1c000
	ds_read_b128 v[0:3], v4
	ds_read_b128 v[16:19], v4 offset:2048
	ds_read_b128 v[4:7], v8
	ds_read_b128 v[20:23], v8 offset:2048
	v_add_u32_e32 v8, s66, v244
	v_add_u32_e32 v9, s66, v245
	ds_read_b128 v[136:139], v8
	ds_read_b128 v[144:147], v8 offset:2048
	ds_read_b128 v[140:143], v9
	ds_read_b128 v[148:151], v9 offset:2048
	s_mov_b32 m0, s33
	ds_read_b128 v[8:11], v250 offset:32768
	ds_read_b128 v[24:27], v250 offset:34816
	ds_read_b128 v[12:15], v251 offset:32768
	ds_read_b128 v[28:31], v251 offset:34816
	ds_read_b128 v[32:35], v250 offset:36864
	ds_read_b128 v[40:43], v250 offset:38912
	ds_read_b128 v[36:39], v251 offset:36864
	ds_read_b128 v[44:47], v251 offset:38912
	buffer_load_dwordx4 v248, s[8:11], s65 offen lds
	s_mov_b32 m0, s34
	s_nop 0
	buffer_load_dwordx4 v249, s[8:11], s65 offen lds
	s_waitcnt vmcnt(8)
	s_waitcnt lgkmcnt(0)
	s_barrier
	s_setprio 1
	s_waitcnt lgkmcnt(5)
	v_mfma_f32_16x16x128_f8f6f4 v[124:127], v[0:7], v[8:15], v[124:127]
	v_mfma_f32_16x16x128_f8f6f4 v[120:123], v[16:23], v[8:15], v[120:123]
	s_waitcnt lgkmcnt(4)
	v_mfma_f32_16x16x128_f8f6f4 v[108:111], v[0:7], v[24:31], v[108:111]
	v_mfma_f32_16x16x128_f8f6f4 v[104:107], v[16:23], v[24:31], v[104:107]
	s_waitcnt lgkmcnt(1)
	v_mfma_f32_16x16x128_f8f6f4 v[92:95], v[0:7], v[32:39], v[128:131]
	v_mfma_f32_16x16x128_f8f6f4 v[88:91], v[16:23], v[32:39], v[200:203]
	s_waitcnt lgkmcnt(0)
	v_mfma_f32_16x16x128_f8f6f4 v[76:79], v[0:7], v[40:47], v[204:207]
	v_mfma_f32_16x16x128_f8f6f4 v[72:75], v[16:23], v[40:47], v[208:211]
	s_setprio 0
	s_setprio 1
	v_mfma_f32_16x16x128_f8f6f4 v[116:119], v[136:143], v[8:15], v[116:119]
	v_mfma_f32_16x16x128_f8f6f4 v[112:115], v[144:151], v[8:15], v[112:115]
	v_mfma_f32_16x16x128_f8f6f4 v[100:103], v[136:143], v[24:31], v[100:103]
	v_mfma_f32_16x16x128_f8f6f4 v[96:99], v[144:151], v[24:31], v[96:99]
	v_mfma_f32_16x16x128_f8f6f4 v[84:87], v[136:143], v[32:39], v[168:171]
	v_mfma_f32_16x16x128_f8f6f4 v[80:83], v[144:151], v[32:39], v[172:175]
	v_mfma_f32_16x16x128_f8f6f4 v[68:71], v[136:143], v[40:47], v[176:179]
	v_mfma_f32_16x16x128_f8f6f4 v[64:67], v[144:151], v[40:47], v[180:183]
	s_setprio 0
	s_barrier
	s_mov_b32 m0, s36
	s_add_i32 s65, s63, 0x80
	ds_read_b128 v[32:35], v250 offset:49152
	ds_read_b128 v[152:155], v250 offset:51200
	ds_read_b128 v[36:39], v251 offset:49152
	ds_read_b128 v[156:159], v251 offset:51200
	ds_read_b128 v[160:163], v250 offset:53248
	ds_read_b128 v[168:171], v250 offset:55296
	ds_read_b128 v[164:167], v251 offset:53248
	ds_read_b128 v[172:175], v251 offset:55296
	buffer_load_dwordx4 v132, s[4:7], s65 offen lds
	s_mov_b32 m0, s37
	s_add_i32 s63, s63, 0x40080
	buffer_load_dwordx4 v133, s[4:7], s65 offen lds
	s_mov_b32 m0, s40
	s_nop 0
	buffer_load_dwordx4 v132, s[4:7], s63 offen lds
	s_mov_b32 m0, s41
	s_nop 0
	buffer_load_dwordx4 v133, s[4:7], s63 offen lds
	s_mov_b32 m0, s38
	s_nop 0
	buffer_load_dwordx4 v246, s[8:11], s64 offen lds
	s_mov_b32 m0, s39
	s_nop 0
	buffer_load_dwordx4 v247, s[8:11], s64 offen lds
	s_waitcnt vmcnt(8)
	s_waitcnt lgkmcnt(0)
	s_barrier
	s_setprio 1
	s_waitcnt lgkmcnt(5)
	v_mfma_f32_16x16x128_f8f6f4 v[60:63], v[0:7], v[32:39], v[60:63]
	v_mfma_f32_16x16x128_f8f6f4 v[56:59], v[16:23], v[32:39], v[56:59]
	s_waitcnt lgkmcnt(4)
	v_mfma_f32_16x16x128_f8f6f4 v[44:47], v[0:7], v[152:159], v[184:187]
	v_mfma_f32_16x16x128_f8f6f4 v[40:43], v[16:23], v[152:159], v[188:191]
	s_waitcnt lgkmcnt(1)
	v_mfma_f32_16x16x128_f8f6f4 v[28:31], v[0:7], v[160:167], v[192:195]
	v_mfma_f32_16x16x128_f8f6f4 v[24:27], v[16:23], v[160:167], v[196:199]
	s_waitcnt lgkmcnt(0)
	v_mfma_f32_16x16x128_f8f6f4 v[12:15], v[0:7], v[168:175], v[212:215]
	v_mfma_f32_16x16x128_f8f6f4 v[8:11], v[16:23], v[168:175], v[216:219]
	s_setprio 0
	s_setprio 1
	v_mfma_f32_16x16x128_f8f6f4 v[52:55], v[136:143], v[32:39], v[52:55]
	v_mfma_f32_16x16x128_f8f6f4 v[48:51], v[144:151], v[32:39], v[48:51]
	v_mfma_f32_16x16x128_f8f6f4 v[36:39], v[136:143], v[152:159], v[220:223]
	v_mfma_f32_16x16x128_f8f6f4 v[32:35], v[144:151], v[152:159], v[224:227]
	v_mfma_f32_16x16x128_f8f6f4 v[20:23], v[136:143], v[160:167], v[228:231]
	v_mfma_f32_16x16x128_f8f6f4 v[16:19], v[144:151], v[160:167], v[232:235]
	v_mfma_f32_16x16x128_f8f6f4 v[4:7], v[136:143], v[168:175], v[236:239]
	v_mfma_f32_16x16x128_f8f6f4 v[0:3], v[144:151], v[168:175], v[240:243]
	s_setprio 0
	s_barrier
	s_add_i32 s61, s61, 2
	s_addk_i32 s62, 0x100
	s_cmp_gt_u32 s61, 13
	s_cbranch_scc1 .LBB0_2177

.LBB0_2197:
	v_add_u32_e32 v129, s19, v128
	v_ashrrev_i32_e32 v131, 3, v129
	v_lshlrev_b32_e32 v130, 4, v128
	v_lshlrev_b32_e32 v132, 1, v131
	v_lshrrev_b32_e32 v133, 2, v131
	v_bitop3_b32 v130, v129, s24, v130 bitop3:0x48
	v_and_b32_e32 v132, 24, v132
	v_and_b32_e32 v133, 4, v133
	v_and_b32_e32 v134, 0x1fffe3, v131
	v_lshl_add_u32 v129, v129, 4, v156
	v_or3_b32 v132, v134, v133, v132
	v_ashrrev_i32_e32 v129, 7, v129
	v_lshl_or_b32 v159, v132, 11, v130
	v_lshlrev_b32_e32 v132, 1, v129
	v_lshrrev_b32_e32 v133, 2, v129
	v_and_b32_e32 v132, 24, v132
	v_and_b32_e32 v133, 4, v133
	v_and_b32_e32 v134, 0x1fffe3, v129
	v_or3_b32 v132, v134, v133, v132
	v_lshrrev_b32_e32 v133, 3, v128
	v_lshl_or_b32 v244, v132, 11, v130
	v_and_b32_e32 v132, 15, v128
	v_and_b32_e32 v134, 0xffffffe, v133
	v_bfe_u32 v128, v128, 1, 3
	v_lshlrev_b32_e32 v132, 7, v132
	v_bitop3_b32 v133, v133, v128, s50 bitop3:0x6c
	v_bitop3_b32 v128, v134, v128, 1 bitop3:0x36
	v_or_b32_e32 v152, s44, v132
	v_or_b32_e32 v132, s45, v132
	v_lshlrev_b32_e32 v153, 4, v133
	v_lshlrev_b32_e32 v154, 4, v128
	v_add_u32_e32 v245, v153, v132
	v_add_u32_e32 v246, v154, v132
	v_add_u32_e32 v132, s51, v245
	v_add_u32_e32 v140, s51, v246
	v_add_u32_e32 v148, s52, v245
	v_lshl_or_b32 v247, v131, 11, v130
	v_lshl_or_b32 v248, v129, 11, v130
	ds_read_b128 v[128:131], v132
	ds_read_b128 v[136:139], v132 offset:2048
	ds_read_b128 v[132:135], v140
	ds_read_b128 v[140:143], v140 offset:2048
	v_add_u32_e32 v155, s52, v246
	ds_read_b128 v[144:147], v148
	ds_read_b128 v[160:163], v148 offset:2048
	ds_read_b128 v[148:151], v155
	ds_read_b128 v[164:167], v155 offset:2048
	s_add_i32 s6, s64, 0xffffff80
	s_add_i32 s7, s6, s59
	s_cmpk_eq_i32 s64, 0x880
	s_cselect_b32 s67, s37, s56
	s_cselect_b32 s6, 0, s6
	s_cselect_b32 s66, 0x80, s64
	s_cselect_b32 s65, s31, s7
	s_add_i32 s7, s56, s64
	v_add_u32_e32 v249, 0x40000, v247
	v_add_u32_e32 v250, 0x40000, v248
	s_add_i32 s66, s67, s66
	s_addk_i32 s7, 0xff00
	s_add_i32 s67, s67, s6
	v_add3_u32 v251, v153, v152, 0
	s_mov_b32 m0, s46
	v_add3_u32 v252, v154, v152, 0
	ds_read_b128 v[168:171], v251
	ds_read_b128 v[176:179], v251 offset:2048
	ds_read_b128 v[172:175], v252
	ds_read_b128 v[180:183], v252 offset:2048
	ds_read_b128 v[184:187], v251 offset:4096
	ds_read_b128 v[192:195], v251 offset:6144
	ds_read_b128 v[188:191], v252 offset:4096
	ds_read_b128 v[196:199], v252 offset:6144
	buffer_load_dwordx4 v249, s[8:11], s7 offen lds
	s_mov_b32 m0, s49
	s_nop 0
	buffer_load_dwordx4 v250, s[8:11], s7 offen lds
	s_waitcnt vmcnt(8)
	s_waitcnt lgkmcnt(0)
	s_barrier
	s_setprio 1
	s_waitcnt lgkmcnt(5)
	v_mfma_f32_16x16x128_f8f6f4 v[124:127], v[128:135], v[168:175], v[124:127]
	v_mfma_f32_16x16x128_f8f6f4 v[120:123], v[136:143], v[168:175], v[120:123]
	s_waitcnt lgkmcnt(4)
	v_mfma_f32_16x16x128_f8f6f4 v[108:111], v[128:135], v[176:183], v[108:111]
	v_mfma_f32_16x16x128_f8f6f4 v[104:107], v[136:143], v[176:183], v[104:107]
	s_waitcnt lgkmcnt(1)
	v_mfma_f32_16x16x128_f8f6f4 v[152:155], v[128:135], v[184:191], v[92:95]
	v_mfma_f32_16x16x128_f8f6f4 v[200:203], v[136:143], v[184:191], v[88:91]
	s_waitcnt lgkmcnt(0)
	v_mfma_f32_16x16x128_f8f6f4 v[204:207], v[128:135], v[192:199], v[76:79]
	v_mfma_f32_16x16x128_f8f6f4 v[208:211], v[136:143], v[192:199], v[72:75]
	s_setprio 0
	s_setprio 1
	v_mfma_f32_16x16x128_f8f6f4 v[116:119], v[144:151], v[168:175], v[116:119]
	v_mfma_f32_16x16x128_f8f6f4 v[112:115], v[160:167], v[168:175], v[112:115]
	v_mfma_f32_16x16x128_f8f6f4 v[100:103], v[144:151], v[176:183], v[100:103]
	v_mfma_f32_16x16x128_f8f6f4 v[96:99], v[160:167], v[176:183], v[96:99]
	v_mfma_f32_16x16x128_f8f6f4 v[168:171], v[144:151], v[184:191], v[84:87]
	v_mfma_f32_16x16x128_f8f6f4 v[172:175], v[160:167], v[184:191], v[80:83]
	v_mfma_f32_16x16x128_f8f6f4 v[176:179], v[144:151], v[192:199], v[68:71]
	v_mfma_f32_16x16x128_f8f6f4 v[180:183], v[160:167], v[192:199], v[64:67]
	s_setprio 0
	s_barrier
	s_mov_b32 m0, s28
	s_mov_b32 s6, s10
	s_mov_b32 s7, s11
	s_nop 1
	ds_read_b128 v[64:67], v251 offset:16384
	ds_read_b128 v[72:75], v251 offset:18432
	ds_read_b128 v[68:71], v252 offset:16384
	ds_read_b128 v[76:79], v252 offset:18432
	ds_read_b128 v[80:83], v251 offset:20480
	ds_read_b128 v[88:91], v251 offset:22528
	ds_read_b128 v[84:87], v252 offset:20480
	ds_read_b128 v[92:95], v252 offset:22528
	buffer_load_dwordx4 v159, s[4:7], s65 offen lds
	s_mov_b32 m0, s29
	s_add_i32 s68, s65, 0x40000
	buffer_load_dwordx4 v244, s[4:7], s65 offen lds
	s_mov_b32 m0, s30
	s_nop 0
	buffer_load_dwordx4 v159, s[4:7], s68 offen lds
	s_mov_b32 m0, s33
	s_nop 0
	buffer_load_dwordx4 v244, s[4:7], s68 offen lds
	s_mov_b32 m0, s27
	s_nop 0
	buffer_load_dwordx4 v247, s[8:11], s67 offen lds
	s_mov_b32 m0, s34
	s_nop 0
	buffer_load_dwordx4 v248, s[8:11], s67 offen lds
	s_waitcnt vmcnt(8)
	s_waitcnt lgkmcnt(0)
	s_barrier
	s_setprio 1
	s_waitcnt lgkmcnt(5)
	v_mfma_f32_16x16x128_f8f6f4 v[60:63], v[128:135], v[64:71], v[60:63]
	v_mfma_f32_16x16x128_f8f6f4 v[56:59], v[136:143], v[64:71], v[56:59]
	s_waitcnt lgkmcnt(4)
	v_mfma_f32_16x16x128_f8f6f4 v[184:187], v[128:135], v[72:79], v[44:47]
	v_mfma_f32_16x16x128_f8f6f4 v[188:191], v[136:143], v[72:79], v[40:43]
	s_waitcnt lgkmcnt(1)
	v_mfma_f32_16x16x128_f8f6f4 v[192:195], v[128:135], v[80:87], v[28:31]
	v_mfma_f32_16x16x128_f8f6f4 v[196:199], v[136:143], v[80:87], v[24:27]
	s_waitcnt lgkmcnt(0)
	v_mfma_f32_16x16x128_f8f6f4 v[212:215], v[128:135], v[88:95], v[12:15]
	v_mfma_f32_16x16x128_f8f6f4 v[216:219], v[136:143], v[88:95], v[8:11]
	s_setprio 0
	s_setprio 1
	v_mfma_f32_16x16x128_f8f6f4 v[52:55], v[144:151], v[64:71], v[52:55]
	v_mfma_f32_16x16x128_f8f6f4 v[48:51], v[160:167], v[64:71], v[48:51]
	v_mfma_f32_16x16x128_f8f6f4 v[220:223], v[144:151], v[72:79], v[36:39]
	v_mfma_f32_16x16x128_f8f6f4 v[224:227], v[160:167], v[72:79], v[32:35]
	v_mfma_f32_16x16x128_f8f6f4 v[228:231], v[144:151], v[80:87], v[20:23]
	v_mfma_f32_16x16x128_f8f6f4 v[232:235], v[160:167], v[80:87], v[16:19]
	v_mfma_f32_16x16x128_f8f6f4 v[236:239], v[144:151], v[88:95], v[4:7]
	v_mfma_f32_16x16x128_f8f6f4 v[240:243], v[160:167], v[88:95], v[0:3]
	s_setprio 0
	s_barrier
	s_add_i32 s68, 0, 0x18000
	s_nop 2
	v_add_u32_e32 v4, s68, v245
	v_add_u32_e32 v8, s68, v246
	s_add_i32 s68, 0, 0x1c000
	ds_read_b128 v[0:3], v4
	ds_read_b128 v[16:19], v4 offset:2048
	ds_read_b128 v[4:7], v8
	ds_read_b128 v[20:23], v8 offset:2048
	v_add_u32_e32 v8, s68, v245
	v_add_u32_e32 v9, s68, v246
	ds_read_b128 v[128:131], v8
	ds_read_b128 v[136:139], v8 offset:2048
	ds_read_b128 v[132:135], v9
	ds_read_b128 v[140:143], v9 offset:2048
	s_mov_b32 m0, s35
	ds_read_b128 v[8:11], v251 offset:32768
	ds_read_b128 v[24:27], v251 offset:34816
	ds_read_b128 v[12:15], v252 offset:32768
	ds_read_b128 v[28:31], v252 offset:34816
	ds_read_b128 v[32:35], v251 offset:36864
	ds_read_b128 v[40:43], v251 offset:38912
	ds_read_b128 v[36:39], v252 offset:36864
	ds_read_b128 v[44:47], v252 offset:38912
	buffer_load_dwordx4 v249, s[8:11], s67 offen lds
	s_mov_b32 m0, s36
	s_nop 0
	buffer_load_dwordx4 v250, s[8:11], s67 offen lds
	s_waitcnt vmcnt(8)
	s_waitcnt lgkmcnt(0)
	s_barrier
	s_setprio 1
	s_waitcnt lgkmcnt(5)
	v_mfma_f32_16x16x128_f8f6f4 v[124:127], v[0:7], v[8:15], v[124:127]
	v_mfma_f32_16x16x128_f8f6f4 v[120:123], v[16:23], v[8:15], v[120:123]
	s_waitcnt lgkmcnt(4)
	v_mfma_f32_16x16x128_f8f6f4 v[108:111], v[0:7], v[24:31], v[108:111]
	v_mfma_f32_16x16x128_f8f6f4 v[104:107], v[16:23], v[24:31], v[104:107]
	s_waitcnt lgkmcnt(1)
	v_mfma_f32_16x16x128_f8f6f4 v[92:95], v[0:7], v[32:39], v[152:155]
	v_mfma_f32_16x16x128_f8f6f4 v[88:91], v[16:23], v[32:39], v[200:203]
	s_waitcnt lgkmcnt(0)
	v_mfma_f32_16x16x128_f8f6f4 v[76:79], v[0:7], v[40:47], v[204:207]
	v_mfma_f32_16x16x128_f8f6f4 v[72:75], v[16:23], v[40:47], v[208:211]
	s_setprio 0
	s_setprio 1
	v_mfma_f32_16x16x128_f8f6f4 v[116:119], v[128:135], v[8:15], v[116:119]
	v_mfma_f32_16x16x128_f8f6f4 v[112:115], v[136:143], v[8:15], v[112:115]
	v_mfma_f32_16x16x128_f8f6f4 v[100:103], v[128:135], v[24:31], v[100:103]
	v_mfma_f32_16x16x128_f8f6f4 v[96:99], v[136:143], v[24:31], v[96:99]
	v_mfma_f32_16x16x128_f8f6f4 v[84:87], v[128:135], v[32:39], v[168:171]
	v_mfma_f32_16x16x128_f8f6f4 v[80:83], v[136:143], v[32:39], v[172:175]
	v_mfma_f32_16x16x128_f8f6f4 v[68:71], v[128:135], v[40:47], v[176:179]
	v_mfma_f32_16x16x128_f8f6f4 v[64:67], v[136:143], v[40:47], v[180:183]
	s_setprio 0
	s_barrier
	s_mov_b32 m0, s38
	s_add_i32 s67, s65, 0x80
	ds_read_b128 v[32:35], v251 offset:49152
	ds_read_b128 v[144:147], v251 offset:51200
	ds_read_b128 v[36:39], v252 offset:49152
	ds_read_b128 v[148:151], v252 offset:51200
	ds_read_b128 v[160:163], v251 offset:53248
	ds_read_b128 v[168:171], v251 offset:55296
	ds_read_b128 v[164:167], v252 offset:53248
	ds_read_b128 v[172:175], v252 offset:55296
	buffer_load_dwordx4 v159, s[4:7], s67 offen lds
	s_mov_b32 m0, s39
	s_add_i32 s65, s65, 0x40080
	buffer_load_dwordx4 v244, s[4:7], s67 offen lds
	s_mov_b32 m0, s42
	s_nop 0
	buffer_load_dwordx4 v159, s[4:7], s65 offen lds
	s_mov_b32 m0, s43
	s_nop 0
	buffer_load_dwordx4 v244, s[4:7], s65 offen lds
	s_mov_b32 m0, s40
	s_nop 0
	buffer_load_dwordx4 v247, s[8:11], s66 offen lds
	s_mov_b32 m0, s41
	s_nop 0
	buffer_load_dwordx4 v248, s[8:11], s66 offen lds
	s_waitcnt vmcnt(8)
	s_waitcnt lgkmcnt(0)
	s_barrier
	s_setprio 1
	s_waitcnt lgkmcnt(5)
	v_mfma_f32_16x16x128_f8f6f4 v[60:63], v[0:7], v[32:39], v[60:63]
	v_mfma_f32_16x16x128_f8f6f4 v[56:59], v[16:23], v[32:39], v[56:59]
	s_waitcnt lgkmcnt(4)
	v_mfma_f32_16x16x128_f8f6f4 v[44:47], v[0:7], v[144:151], v[184:187]
	v_mfma_f32_16x16x128_f8f6f4 v[40:43], v[16:23], v[144:151], v[188:191]
	s_waitcnt lgkmcnt(1)
	v_mfma_f32_16x16x128_f8f6f4 v[28:31], v[0:7], v[160:167], v[192:195]
	v_mfma_f32_16x16x128_f8f6f4 v[24:27], v[16:23], v[160:167], v[196:199]
	s_waitcnt lgkmcnt(0)
	v_mfma_f32_16x16x128_f8f6f4 v[12:15], v[0:7], v[168:175], v[212:215]
	v_mfma_f32_16x16x128_f8f6f4 v[8:11], v[16:23], v[168:175], v[216:219]
	s_setprio 0
	s_setprio 1
	v_mfma_f32_16x16x128_f8f6f4 v[52:55], v[128:135], v[32:39], v[52:55]
	v_mfma_f32_16x16x128_f8f6f4 v[48:51], v[136:143], v[32:39], v[48:51]
	v_mfma_f32_16x16x128_f8f6f4 v[36:39], v[128:135], v[144:151], v[220:223]
	v_mfma_f32_16x16x128_f8f6f4 v[32:35], v[136:143], v[144:151], v[224:227]
	v_mfma_f32_16x16x128_f8f6f4 v[20:23], v[128:135], v[160:167], v[228:231]
	v_mfma_f32_16x16x128_f8f6f4 v[16:19], v[136:143], v[160:167], v[232:235]
	v_mfma_f32_16x16x128_f8f6f4 v[4:7], v[128:135], v[168:175], v[236:239]
	v_mfma_f32_16x16x128_f8f6f4 v[0:3], v[136:143], v[168:175], v[240:243]
	s_setprio 0
	s_barrier
	s_add_i32 s63, s63, 2
	s_addk_i32 s64, 0x100
	s_cmp_gt_u32 s63, 13
	s_cbranch_scc1 .LBB0_2201

.LBB0_2275:
	v_add_u32_e32 v129, s17, v128
	v_ashrrev_i32_e32 v131, 3, v129
	v_lshlrev_b32_e32 v130, 4, v128
	v_lshlrev_b32_e32 v132, 1, v131
	v_lshrrev_b32_e32 v133, 2, v131
	v_bitop3_b32 v130, v129, s22, v130 bitop3:0x48
	v_and_b32_e32 v132, 24, v132
	v_and_b32_e32 v133, 4, v133
	v_and_b32_e32 v134, 0x1fffe3, v131
	v_lshl_add_u32 v129, v129, 4, v136
	v_or3_b32 v132, v134, v133, v132
	v_ashrrev_i32_e32 v129, 7, v129
	v_lshl_or_b32 v242, v132, 11, v130
	v_lshlrev_b32_e32 v132, 1, v129
	v_lshrrev_b32_e32 v133, 2, v129
	v_and_b32_e32 v132, 24, v132
	v_and_b32_e32 v133, 4, v133
	v_and_b32_e32 v134, 0x1fffe3, v129
	v_or3_b32 v132, v134, v133, v132
	v_lshrrev_b32_e32 v133, 3, v128
	v_lshl_or_b32 v243, v132, 11, v130
	v_and_b32_e32 v132, 15, v128
	v_and_b32_e32 v134, 0xffffffe, v133
	v_bfe_u32 v128, v128, 1, 3
	v_lshlrev_b32_e32 v132, 7, v132
	v_bitop3_b32 v133, v133, v128, s48 bitop3:0x6c
	v_bitop3_b32 v128, v134, v128, 1 bitop3:0x36
	v_or_b32_e32 v162, s42, v132
	v_or_b32_e32 v132, s43, v132
	v_lshlrev_b32_e32 v163, 4, v133
	v_lshlrev_b32_e32 v164, 4, v128
	v_add_u32_e32 v244, v163, v132
	v_add_u32_e32 v245, v164, v132
	v_add_u32_e32 v132, s49, v244
	v_add_u32_e32 v142, s49, v245
	v_add_u32_e32 v150, s50, v244
	v_add_u32_e32 v158, s50, v245
	v_lshl_or_b32 v246, v131, 11, v130
	v_lshl_or_b32 v247, v129, 11, v130
	ds_read_b128 v[128:131], v132
	ds_read_b128 v[138:141], v132 offset:2048
	ds_read_b128 v[132:135], v142
	ds_read_b128 v[142:145], v142 offset:2048
	ds_read_b128 v[146:149], v150
	ds_read_b128 v[154:157], v150 offset:2048
	ds_read_b128 v[150:153], v158
	ds_read_b128 v[158:161], v158 offset:2048
	s_add_i32 s6, s61, 0xffffff80
	s_add_i32 s7, s6, s56
	s_cmpk_eq_i32 s61, 0x880
	s_cselect_b32 s64, s35, s53
	s_cselect_b32 s6, 0, s6
	s_cselect_b32 s63, 0x80, s61
	s_cselect_b32 s62, s29, s7
	s_add_i32 s7, s53, s61
	v_add_u32_e32 v248, 0x40000, v246
	v_add_u32_e32 v249, 0x40000, v247
	s_add_i32 s63, s64, s63
	s_addk_i32 s7, 0xff00
	s_add_i32 s64, s64, s6
	v_add3_u32 v250, v163, v162, 0
	s_mov_b32 m0, s44
	v_add3_u32 v251, v164, v162, 0
	ds_read_b128 v[162:165], v250
	ds_read_b128 v[170:173], v250 offset:2048
	ds_read_b128 v[166:169], v251
	ds_read_b128 v[174:177], v251 offset:2048
	ds_read_b128 v[178:181], v250 offset:4096
	ds_read_b128 v[186:189], v250 offset:6144
	ds_read_b128 v[182:185], v251 offset:4096
	ds_read_b128 v[190:193], v251 offset:6144
	buffer_load_dwordx4 v248, s[8:11], s7 offen lds
	s_mov_b32 m0, s47
	s_nop 0
	buffer_load_dwordx4 v249, s[8:11], s7 offen lds
	s_waitcnt vmcnt(8)
	s_waitcnt lgkmcnt(0)
	s_barrier
	s_setprio 1
	s_waitcnt lgkmcnt(0)
	v_mfma_f32_16x16x128_f8f6f4 v[124:127], v[128:135], v[162:169], v[124:127]
	v_mfma_f32_16x16x128_f8f6f4 v[120:123], v[138:145], v[162:169], v[120:123]
	v_mfma_f32_16x16x128_f8f6f4 v[116:119], v[128:135], v[170:177], v[116:119]
	v_mfma_f32_16x16x128_f8f6f4 v[112:115], v[138:145], v[170:177], v[112:115]
	v_mfma_f32_16x16x128_f8f6f4 v[194:197], v[128:135], v[178:185], v[92:95]
	v_mfma_f32_16x16x128_f8f6f4 v[198:201], v[138:145], v[178:185], v[88:91]
	v_mfma_f32_16x16x128_f8f6f4 v[202:205], v[128:135], v[186:193], v[84:87]
	v_mfma_f32_16x16x128_f8f6f4 v[206:209], v[138:145], v[186:193], v[80:83]
	s_setprio 0
	s_setprio 1
	v_mfma_f32_16x16x128_f8f6f4 v[108:111], v[146:153], v[162:169], v[108:111]
	v_mfma_f32_16x16x128_f8f6f4 v[104:107], v[154:161], v[162:169], v[104:107]
	v_mfma_f32_16x16x128_f8f6f4 v[100:103], v[146:153], v[170:177], v[100:103]
	v_mfma_f32_16x16x128_f8f6f4 v[96:99], v[154:161], v[170:177], v[96:99]
	v_mfma_f32_16x16x128_f8f6f4 v[162:165], v[146:153], v[178:185], v[76:79]
	v_mfma_f32_16x16x128_f8f6f4 v[166:169], v[154:161], v[178:185], v[72:75]
	v_mfma_f32_16x16x128_f8f6f4 v[170:173], v[146:153], v[186:193], v[68:71]
	v_mfma_f32_16x16x128_f8f6f4 v[174:177], v[154:161], v[186:193], v[64:67]
	s_setprio 0
	s_barrier
	s_mov_b32 m0, s26
	s_mov_b32 s6, s10
	s_mov_b32 s7, s11
	s_nop 1
	ds_read_b128 v[64:67], v250 offset:16384
	ds_read_b128 v[72:75], v250 offset:18432
	ds_read_b128 v[68:71], v251 offset:16384
	ds_read_b128 v[76:79], v251 offset:18432
	ds_read_b128 v[80:83], v250 offset:20480
	ds_read_b128 v[88:91], v250 offset:22528
	ds_read_b128 v[84:87], v251 offset:20480
	ds_read_b128 v[92:95], v251 offset:22528
	buffer_load_dwordx4 v242, s[4:7], s62 offen lds
	s_mov_b32 m0, s27
	s_add_i32 s65, s62, 0x40000
	buffer_load_dwordx4 v243, s[4:7], s62 offen lds
	s_mov_b32 m0, s28
	s_nop 0
	buffer_load_dwordx4 v242, s[4:7], s65 offen lds
	s_mov_b32 m0, s30
	s_nop 0
	buffer_load_dwordx4 v243, s[4:7], s65 offen lds
	s_mov_b32 m0, s25
	s_nop 0
	buffer_load_dwordx4 v246, s[8:11], s64 offen lds
	s_mov_b32 m0, s31
	s_nop 0
	buffer_load_dwordx4 v247, s[8:11], s64 offen lds
	s_waitcnt vmcnt(8)
	s_waitcnt lgkmcnt(0)
	s_barrier
	s_setprio 1
	s_waitcnt lgkmcnt(5)
	v_mfma_f32_16x16x128_f8f6f4 v[60:63], v[128:135], v[64:71], v[60:63]
	v_mfma_f32_16x16x128_f8f6f4 v[56:59], v[138:145], v[64:71], v[56:59]
	s_waitcnt lgkmcnt(4)
	v_mfma_f32_16x16x128_f8f6f4 v[52:55], v[128:135], v[72:79], v[52:55]
	v_mfma_f32_16x16x128_f8f6f4 v[48:51], v[138:145], v[72:79], v[48:51]
	s_waitcnt lgkmcnt(1)
	v_mfma_f32_16x16x128_f8f6f4 v[178:181], v[128:135], v[80:87], v[28:31]
	v_mfma_f32_16x16x128_f8f6f4 v[182:185], v[138:145], v[80:87], v[24:27]
	s_waitcnt lgkmcnt(0)
	v_mfma_f32_16x16x128_f8f6f4 v[186:189], v[128:135], v[88:95], v[20:23]
	v_mfma_f32_16x16x128_f8f6f4 v[190:193], v[138:145], v[88:95], v[16:19]
	s_setprio 0
	s_setprio 1
	v_mfma_f32_16x16x128_f8f6f4 v[210:213], v[146:153], v[64:71], v[44:47]
	v_mfma_f32_16x16x128_f8f6f4 v[214:217], v[154:161], v[64:71], v[40:43]
	v_mfma_f32_16x16x128_f8f6f4 v[218:221], v[146:153], v[72:79], v[36:39]
	v_mfma_f32_16x16x128_f8f6f4 v[222:225], v[154:161], v[72:79], v[32:35]
	v_mfma_f32_16x16x128_f8f6f4 v[226:229], v[146:153], v[80:87], v[12:15]
	v_mfma_f32_16x16x128_f8f6f4 v[230:233], v[154:161], v[80:87], v[8:11]
	v_mfma_f32_16x16x128_f8f6f4 v[234:237], v[146:153], v[88:95], v[4:7]
	v_mfma_f32_16x16x128_f8f6f4 v[238:241], v[154:161], v[88:95], v[0:3]
	s_setprio 0
	s_barrier
	s_add_i32 s65, 0, 0x18000
	s_nop 2
	v_add_u32_e32 v4, s65, v244
	v_add_u32_e32 v12, s65, v245
	s_add_i32 s65, 0, 0x1c000
	v_add_u32_e32 v16, s65, v244
	ds_read_b128 v[0:3], v4
	ds_read_b128 v[8:11], v4 offset:2048
	ds_read_b128 v[4:7], v12
	ds_read_b128 v[12:15], v12 offset:2048
	v_add_u32_e32 v17, s65, v245
	ds_read_b128 v[128:131], v16
	ds_read_b128 v[138:141], v16 offset:2048
	ds_read_b128 v[132:135], v17
	ds_read_b128 v[142:145], v17 offset:2048
	s_mov_b32 m0, s33
	ds_read_b128 v[16:19], v250 offset:32768
	ds_read_b128 v[24:27], v250 offset:34816
	ds_read_b128 v[20:23], v251 offset:32768
	ds_read_b128 v[28:31], v251 offset:34816
	ds_read_b128 v[32:35], v250 offset:36864
	ds_read_b128 v[40:43], v250 offset:38912
	ds_read_b128 v[36:39], v251 offset:36864
	ds_read_b128 v[44:47], v251 offset:38912
	buffer_load_dwordx4 v248, s[8:11], s64 offen lds
	s_mov_b32 m0, s34
	s_nop 0
	buffer_load_dwordx4 v249, s[8:11], s64 offen lds
	s_waitcnt vmcnt(8)
	s_waitcnt lgkmcnt(0)
	s_barrier
	s_setprio 1
	s_waitcnt lgkmcnt(5)
	v_mfma_f32_16x16x128_f8f6f4 v[124:127], v[0:7], v[16:23], v[124:127]
	v_mfma_f32_16x16x128_f8f6f4 v[120:123], v[8:15], v[16:23], v[120:123]
	s_waitcnt lgkmcnt(4)
	v_mfma_f32_16x16x128_f8f6f4 v[116:119], v[0:7], v[24:31], v[116:119]
	v_mfma_f32_16x16x128_f8f6f4 v[112:115], v[8:15], v[24:31], v[112:115]
	s_waitcnt lgkmcnt(1)
	v_mfma_f32_16x16x128_f8f6f4 v[92:95], v[0:7], v[32:39], v[194:197]
	v_mfma_f32_16x16x128_f8f6f4 v[88:91], v[8:15], v[32:39], v[198:201]
	s_waitcnt lgkmcnt(0)
	v_mfma_f32_16x16x128_f8f6f4 v[84:87], v[0:7], v[40:47], v[202:205]
	v_mfma_f32_16x16x128_f8f6f4 v[80:83], v[8:15], v[40:47], v[206:209]
	s_setprio 0
	s_setprio 1
	v_mfma_f32_16x16x128_f8f6f4 v[108:111], v[128:135], v[16:23], v[108:111]
	v_mfma_f32_16x16x128_f8f6f4 v[104:107], v[138:145], v[16:23], v[104:107]
	v_mfma_f32_16x16x128_f8f6f4 v[100:103], v[128:135], v[24:31], v[100:103]
	v_mfma_f32_16x16x128_f8f6f4 v[96:99], v[138:145], v[24:31], v[96:99]
	v_mfma_f32_16x16x128_f8f6f4 v[76:79], v[128:135], v[32:39], v[162:165]
	v_mfma_f32_16x16x128_f8f6f4 v[72:75], v[138:145], v[32:39], v[166:169]
	v_mfma_f32_16x16x128_f8f6f4 v[68:71], v[128:135], v[40:47], v[170:173]
	v_mfma_f32_16x16x128_f8f6f4 v[64:67], v[138:145], v[40:47], v[174:177]
	s_setprio 0
	s_barrier
	s_mov_b32 m0, s36
	s_add_i32 s64, s62, 0x80
	ds_read_b128 v[32:35], v250 offset:49152
	ds_read_b128 v[146:149], v250 offset:51200
	ds_read_b128 v[36:39], v251 offset:49152
	ds_read_b128 v[150:153], v251 offset:51200
	ds_read_b128 v[154:157], v250 offset:53248
	ds_read_b128 v[162:165], v250 offset:55296
	ds_read_b128 v[158:161], v251 offset:53248
	ds_read_b128 v[166:169], v251 offset:55296
	buffer_load_dwordx4 v242, s[4:7], s64 offen lds
	s_mov_b32 m0, s37
	s_add_i32 s62, s62, 0x40080
	buffer_load_dwordx4 v243, s[4:7], s64 offen lds
	s_mov_b32 m0, s40
	s_nop 0
	buffer_load_dwordx4 v242, s[4:7], s62 offen lds
	s_mov_b32 m0, s41
	s_nop 0
	buffer_load_dwordx4 v243, s[4:7], s62 offen lds
	s_mov_b32 m0, s38
	s_nop 0
	buffer_load_dwordx4 v246, s[8:11], s63 offen lds
	s_mov_b32 m0, s39
	s_nop 0
	buffer_load_dwordx4 v247, s[8:11], s63 offen lds
	s_waitcnt vmcnt(8)
	s_waitcnt lgkmcnt(0)
	s_barrier
	s_setprio 1
	s_waitcnt lgkmcnt(5)
	v_mfma_f32_16x16x128_f8f6f4 v[60:63], v[0:7], v[32:39], v[60:63]
	v_mfma_f32_16x16x128_f8f6f4 v[56:59], v[8:15], v[32:39], v[56:59]
	s_waitcnt lgkmcnt(4)
	v_mfma_f32_16x16x128_f8f6f4 v[52:55], v[0:7], v[146:153], v[52:55]
	v_mfma_f32_16x16x128_f8f6f4 v[48:51], v[8:15], v[146:153], v[48:51]
	s_waitcnt lgkmcnt(1)
	v_mfma_f32_16x16x128_f8f6f4 v[28:31], v[0:7], v[154:161], v[178:181]
	v_mfma_f32_16x16x128_f8f6f4 v[24:27], v[8:15], v[154:161], v[182:185]
	s_waitcnt lgkmcnt(0)
	v_mfma_f32_16x16x128_f8f6f4 v[20:23], v[0:7], v[162:169], v[186:189]
	v_mfma_f32_16x16x128_f8f6f4 v[16:19], v[8:15], v[162:169], v[190:193]
	s_setprio 0
	s_setprio 1
	v_mfma_f32_16x16x128_f8f6f4 v[44:47], v[128:135], v[32:39], v[210:213]
	v_mfma_f32_16x16x128_f8f6f4 v[40:43], v[138:145], v[32:39], v[214:217]
	v_mfma_f32_16x16x128_f8f6f4 v[36:39], v[128:135], v[146:153], v[218:221]
	v_mfma_f32_16x16x128_f8f6f4 v[32:35], v[138:145], v[146:153], v[222:225]
	v_mfma_f32_16x16x128_f8f6f4 v[12:15], v[128:135], v[154:161], v[226:229]
	v_mfma_f32_16x16x128_f8f6f4 v[8:11], v[138:145], v[154:161], v[230:233]
	v_mfma_f32_16x16x128_f8f6f4 v[4:7], v[128:135], v[162:169], v[234:237]
	v_mfma_f32_16x16x128_f8f6f4 v[0:3], v[138:145], v[162:169], v[238:241]
	s_setprio 0
	s_barrier
	s_add_i32 s60, s60, 2
	s_addk_i32 s61, 0x100
	s_cmp_gt_u32 s60, 13
	s_cbranch_scc1 .LBB0_2279

.LBB0_2473:
	v_lshlrev_b32_e32 v206, 1, v203
	v_lshrrev_b32_e32 v207, 2, v203
	s_add_i32 s10, s82, 0xffffff80
	v_and_b32_e32 v206, 24, v206
	v_and_b32_e32 v207, 4, v207
	v_and_b32_e32 v203, 0x1fffe3, v203
	s_waitcnt vmcnt(8)
	s_add_i32 s14, s77, 2
	s_add_i32 s11, s10, s76
	v_or3_b32 v203, v203, v207, v206
	v_lshlrev_b32_e32 v206, 1, v202
	v_lshrrev_b32_e32 v207, 2, v202
	s_waitcnt lgkmcnt(0)
	s_and_b64 s[6:7], s[6:7], exec
	v_and_b32_e32 v206, 24, v206
	v_and_b32_e32 v207, 4, v207
	v_and_b32_e32 v202, 0x1fffe3, v202
	s_cselect_b32 s7, s46, s11
	v_or3_b32 v202, v202, v207, v206
	s_cselect_b32 s6, 0x80, s82
	s_cselect_b32 s83, 0, s10
	s_add_i32 s15, s7, 0x80
	v_lshl_or_b32 v203, v203, 11, v201
	v_lshl_or_b32 v201, v202, 11, v201
	s_barrier
	s_setprio 1
	s_waitcnt lgkmcnt(0)
	v_mfma_f32_16x16x128_f8f6f4 v[192:195], v[16:23], v[40:47], v[192:195]
	v_mfma_f32_16x16x128_f8f6f4 v[188:191], v[24:31], v[40:47], v[188:191]
	v_mfma_f32_16x16x128_f8f6f4 v[176:179], v[16:23], v[32:39], v[176:179]
	v_mfma_f32_16x16x128_f8f6f4 v[168:171], v[24:31], v[32:39], v[168:171]
	v_mfma_f32_16x16x128_f8f6f4 v[160:163], v[16:23], v[56:63], v[160:163]
	v_mfma_f32_16x16x128_f8f6f4 v[152:155], v[24:31], v[56:63], v[152:155]
	v_mfma_f32_16x16x128_f8f6f4 v[144:147], v[16:23], v[48:55], v[144:147]
	v_mfma_f32_16x16x128_f8f6f4 v[136:139], v[24:31], v[48:55], v[136:139]
	s_setprio 0
	s_setprio 1
	v_mfma_f32_16x16x128_f8f6f4 v[184:187], v[0:7], v[40:47], v[184:187]
	v_mfma_f32_16x16x128_f8f6f4 v[180:183], v[8:15], v[40:47], v[180:183]
	v_mfma_f32_16x16x128_f8f6f4 v[172:175], v[0:7], v[32:39], v[172:175]
	v_mfma_f32_16x16x128_f8f6f4 v[164:167], v[8:15], v[32:39], v[164:167]
	v_mfma_f32_16x16x128_f8f6f4 v[156:159], v[0:7], v[56:63], v[156:159]
	v_mfma_f32_16x16x128_f8f6f4 v[148:151], v[8:15], v[56:63], v[148:151]
	v_mfma_f32_16x16x128_f8f6f4 v[140:143], v[0:7], v[48:55], v[140:143]
	v_mfma_f32_16x16x128_f8f6f4 v[132:135], v[8:15], v[48:55], v[132:135]
	s_setprio 0
	s_barrier
	s_mov_b32 m0, s50
	s_mov_b32 s10, s18
	s_mov_b32 s11, s19
	ds_read_b128 v[32:35], v200 offset:16384
	ds_read_b128 v[40:43], v200 offset:18432
	ds_read_b128 v[36:39], v199 offset:16384
	ds_read_b128 v[44:47], v199 offset:18432
	ds_read_b128 v[48:51], v200 offset:20480
	ds_read_b128 v[56:59], v200 offset:22528
	ds_read_b128 v[52:55], v199 offset:20480
	ds_read_b128 v[60:63], v199 offset:22528
	buffer_load_dwordx4 v203, s[8:11], s7 offen lds
	s_mov_b32 m0, s51
	s_add_i32 s84, s7, 0x40000
	buffer_load_dwordx4 v201, s[8:11], s7 offen lds
	s_mov_b32 m0, s52
	s_nop 0
	buffer_load_dwordx4 v203, s[8:11], s84 offen lds
	s_mov_b32 m0, s53
	s_nop 0
	buffer_load_dwordx4 v201, s[8:11], s84 offen lds
	s_mov_b32 m0, s49
	s_nop 0
	buffer_load_dwordx4 v64, s[16:19], s83 offen lds
	s_mov_b32 m0, s54
	s_nop 0
	buffer_load_dwordx4 v65, s[16:19], s83 offen lds
	s_waitcnt vmcnt(8)
	s_waitcnt lgkmcnt(0)
	s_barrier
	s_setprio 1
	s_waitcnt lgkmcnt(5)
	v_mfma_f32_16x16x128_f8f6f4 v[128:131], v[16:23], v[32:39], v[128:131]
	v_mfma_f32_16x16x128_f8f6f4 v[120:123], v[24:31], v[32:39], v[120:123]
	s_waitcnt lgkmcnt(4)
	v_mfma_f32_16x16x128_f8f6f4 v[112:115], v[16:23], v[40:47], v[112:115]
	v_mfma_f32_16x16x128_f8f6f4 v[104:107], v[24:31], v[40:47], v[104:107]
	s_waitcnt lgkmcnt(1)
	v_mfma_f32_16x16x128_f8f6f4 v[96:99], v[16:23], v[48:55], v[96:99]
	v_mfma_f32_16x16x128_f8f6f4 v[88:91], v[24:31], v[48:55], v[88:91]
	s_waitcnt lgkmcnt(0)
	v_mfma_f32_16x16x128_f8f6f4 v[80:83], v[16:23], v[56:63], v[80:83]
	v_mfma_f32_16x16x128_f8f6f4 v[72:75], v[24:31], v[56:63], v[72:75]
	s_setprio 0
	s_setprio 1
	v_mfma_f32_16x16x128_f8f6f4 v[124:127], v[0:7], v[32:39], v[124:127]
	v_mfma_f32_16x16x128_f8f6f4 v[116:119], v[8:15], v[32:39], v[116:119]
	v_mfma_f32_16x16x128_f8f6f4 v[108:111], v[0:7], v[40:47], v[108:111]
	v_mfma_f32_16x16x128_f8f6f4 v[100:103], v[8:15], v[40:47], v[100:103]
	v_mfma_f32_16x16x128_f8f6f4 v[92:95], v[0:7], v[48:55], v[92:95]
	v_mfma_f32_16x16x128_f8f6f4 v[84:87], v[8:15], v[48:55], v[84:87]
	v_mfma_f32_16x16x128_f8f6f4 v[76:79], v[0:7], v[56:63], v[76:79]
	v_mfma_f32_16x16x128_f8f6f4 v[68:71], v[8:15], v[56:63], v[68:71]
	s_setprio 0
	s_barrier
	s_add_i32 s84, 0, 0x18000
	v_add_u32_e32 v4, s84, v204
	v_add_u32_e32 v12, s84, v205
	s_add_i32 s84, 0, 0x1c000
	v_add_u32_e32 v20, s84, v204
	v_add_u32_e32 v28, s84, v205
	ds_read_b128 v[0:3], v4
	ds_read_b128 v[8:11], v4 offset:2048
	ds_read_b128 v[4:7], v12
	ds_read_b128 v[12:15], v12 offset:2048
	ds_read_b128 v[16:19], v20
	ds_read_b128 v[24:27], v20 offset:2048
	ds_read_b128 v[20:23], v28
	ds_read_b128 v[28:31], v28 offset:2048
	s_mov_b32 m0, s55
	ds_read_b128 v[32:35], v200 offset:32768
	ds_read_b128 v[40:43], v200 offset:34816
	ds_read_b128 v[36:39], v199 offset:32768
	ds_read_b128 v[44:47], v199 offset:34816
	ds_read_b128 v[48:51], v200 offset:36864
	ds_read_b128 v[56:59], v200 offset:38912
	ds_read_b128 v[52:55], v199 offset:36864
	ds_read_b128 v[60:63], v199 offset:38912
	buffer_load_dwordx4 v66, s[16:19], s83 offen lds
	s_mov_b32 m0, s56
	s_nop 0
	buffer_load_dwordx4 v67, s[16:19], s83 offen lds
	s_waitcnt vmcnt(8)
	s_waitcnt lgkmcnt(0)
	s_barrier
	s_setprio 1
	s_waitcnt lgkmcnt(5)
	v_mfma_f32_16x16x128_f8f6f4 v[192:195], v[0:7], v[32:39], v[192:195]
	v_mfma_f32_16x16x128_f8f6f4 v[188:191], v[8:15], v[32:39], v[188:191]
	s_waitcnt lgkmcnt(4)
	v_mfma_f32_16x16x128_f8f6f4 v[176:179], v[0:7], v[40:47], v[176:179]
	v_mfma_f32_16x16x128_f8f6f4 v[168:171], v[8:15], v[40:47], v[168:171]
	s_waitcnt lgkmcnt(1)
	v_mfma_f32_16x16x128_f8f6f4 v[160:163], v[0:7], v[48:55], v[160:163]
	v_mfma_f32_16x16x128_f8f6f4 v[152:155], v[8:15], v[48:55], v[152:155]
	s_waitcnt lgkmcnt(0)
	v_mfma_f32_16x16x128_f8f6f4 v[144:147], v[0:7], v[56:63], v[144:147]
	v_mfma_f32_16x16x128_f8f6f4 v[136:139], v[8:15], v[56:63], v[136:139]
	s_setprio 0
	s_setprio 1
	v_mfma_f32_16x16x128_f8f6f4 v[184:187], v[16:23], v[32:39], v[184:187]
	v_mfma_f32_16x16x128_f8f6f4 v[180:183], v[24:31], v[32:39], v[180:183]
	v_mfma_f32_16x16x128_f8f6f4 v[172:175], v[16:23], v[40:47], v[172:175]
	v_mfma_f32_16x16x128_f8f6f4 v[164:167], v[24:31], v[40:47], v[164:167]
	v_mfma_f32_16x16x128_f8f6f4 v[156:159], v[16:23], v[48:55], v[156:159]
	v_mfma_f32_16x16x128_f8f6f4 v[148:151], v[24:31], v[48:55], v[148:151]
	v_mfma_f32_16x16x128_f8f6f4 v[140:143], v[16:23], v[56:63], v[140:143]
	v_mfma_f32_16x16x128_f8f6f4 v[132:135], v[24:31], v[56:63], v[132:135]
	s_setprio 0
	s_barrier
	s_mov_b32 m0, s58
	ds_read_b128 v[32:35], v200 offset:49152
	ds_read_b128 v[40:43], v200 offset:51200
	ds_read_b128 v[36:39], v199 offset:49152
	ds_read_b128 v[44:47], v199 offset:51200
	ds_read_b128 v[48:51], v200 offset:53248
	ds_read_b128 v[56:59], v200 offset:55296
	ds_read_b128 v[52:55], v199 offset:53248
	ds_read_b128 v[60:63], v199 offset:55296
	buffer_load_dwordx4 v203, s[8:11], s15 offen lds
	s_mov_b32 m0, s59
	s_add_i32 s7, s7, 0x40080
	buffer_load_dwordx4 v201, s[8:11], s15 offen lds
	s_mov_b32 m0, s62
	s_nop 0
	buffer_load_dwordx4 v203, s[8:11], s7 offen lds
	s_mov_b32 m0, s63
	s_nop 0
	buffer_load_dwordx4 v201, s[8:11], s7 offen lds
	s_mov_b32 m0, s60
	s_nop 0
	buffer_load_dwordx4 v64, s[16:19], s6 offen lds
	s_mov_b32 m0, s61
	s_nop 0
	buffer_load_dwordx4 v65, s[16:19], s6 offen lds
	s_waitcnt vmcnt(8)
	s_waitcnt lgkmcnt(0)
	s_barrier
	s_setprio 1
	s_waitcnt lgkmcnt(5)
	v_mfma_f32_16x16x128_f8f6f4 v[128:131], v[0:7], v[32:39], v[128:131]
	v_mfma_f32_16x16x128_f8f6f4 v[120:123], v[8:15], v[32:39], v[120:123]
	s_waitcnt lgkmcnt(4)
	v_mfma_f32_16x16x128_f8f6f4 v[112:115], v[0:7], v[40:47], v[112:115]
	v_mfma_f32_16x16x128_f8f6f4 v[104:107], v[8:15], v[40:47], v[104:107]
	s_waitcnt lgkmcnt(1)
	v_mfma_f32_16x16x128_f8f6f4 v[96:99], v[0:7], v[48:55], v[96:99]
	v_mfma_f32_16x16x128_f8f6f4 v[88:91], v[8:15], v[48:55], v[88:91]
	s_waitcnt lgkmcnt(0)
	v_mfma_f32_16x16x128_f8f6f4 v[80:83], v[0:7], v[56:63], v[80:83]
	v_mfma_f32_16x16x128_f8f6f4 v[72:75], v[8:15], v[56:63], v[72:75]
	s_setprio 0
	s_setprio 1
	v_mfma_f32_16x16x128_f8f6f4 v[124:127], v[16:23], v[32:39], v[124:127]
	v_mfma_f32_16x16x128_f8f6f4 v[116:119], v[24:31], v[32:39], v[116:119]
	v_mfma_f32_16x16x128_f8f6f4 v[108:111], v[16:23], v[40:47], v[108:111]
	v_mfma_f32_16x16x128_f8f6f4 v[100:103], v[24:31], v[40:47], v[100:103]
	v_mfma_f32_16x16x128_f8f6f4 v[92:95], v[16:23], v[48:55], v[92:95]
	v_mfma_f32_16x16x128_f8f6f4 v[84:87], v[24:31], v[48:55], v[84:87]
	v_mfma_f32_16x16x128_f8f6f4 v[76:79], v[16:23], v[56:63], v[76:79]
	v_mfma_f32_16x16x128_f8f6f4 v[68:71], v[24:31], v[56:63], v[68:71]
	s_setprio 0
	s_barrier
	s_addk_i32 s82, 0x100
	s_cmp_gt_u32 s77, 13
	s_cbranch_scc1 .LBB0_2479
	s_mov_b32 s77, s14
	s_branch .LBB0_2454

.LBB0_2568:
	v_add_u32_e32 v129, s36, v128
	v_ashrrev_i32_e32 v131, 3, v129
	v_lshlrev_b32_e32 v130, 4, v128
	v_lshlrev_b32_e32 v132, 1, v131
	v_lshrrev_b32_e32 v133, 2, v131
	v_bitop3_b32 v130, v129, s37, v130 bitop3:0x48
	v_and_b32_e32 v132, 24, v132
	v_and_b32_e32 v133, 4, v133
	v_and_b32_e32 v134, 0x1fffe3, v131
	v_lshl_add_u32 v129, v129, 4, v147
	v_or3_b32 v132, v134, v133, v132
	v_ashrrev_i32_e32 v129, 7, v129
	v_lshl_or_b32 v144, v132, 11, v130
	v_lshlrev_b32_e32 v132, 1, v129
	v_lshrrev_b32_e32 v133, 2, v129
	v_and_b32_e32 v132, 24, v132
	v_and_b32_e32 v133, 4, v133
	v_and_b32_e32 v134, 0x1fffe3, v129
	v_or3_b32 v132, v134, v133, v132
	v_lshrrev_b32_e32 v133, 3, v128
	v_lshl_or_b32 v145, v132, 11, v130
	v_and_b32_e32 v132, 15, v128
	v_and_b32_e32 v134, 0xffffffe, v133
	v_bfe_u32 v128, v128, 1, 3
	v_lshlrev_b32_e32 v132, 7, v132
	v_bitop3_b32 v133, v133, v128, s64 bitop3:0x6c
	v_bitop3_b32 v128, v134, v128, 1 bitop3:0x36
	v_or_b32_e32 v146, s58, v132
	v_or_b32_e32 v132, s59, v132
	v_lshlrev_b32_e32 v148, 4, v133
	v_lshlrev_b32_e32 v151, 4, v128
	v_add_u32_e32 v150, v148, v132
	v_add_u32_e32 v152, v151, v132
	v_add_u32_e32 v132, s65, v150
	v_add_u32_e32 v140, s65, v152
	v_add_u32_e32 v158, s66, v150
	v_add_u32_e32 v166, s66, v152
	v_lshl_or_b32 v250, v131, 11, v130
	v_lshl_or_b32 v251, v129, 11, v130
	ds_read_b128 v[128:131], v132
	ds_read_b128 v[136:139], v132 offset:2048
	ds_read_b128 v[132:135], v140
	ds_read_b128 v[140:143], v140 offset:2048
	ds_read_b128 v[154:157], v158
	ds_read_b128 v[162:165], v158 offset:2048
	ds_read_b128 v[158:161], v166
	ds_read_b128 v[166:169], v166 offset:2048
	s_add_i32 s6, s80, 0xffffff80
	s_add_i32 s7, s6, s75
	s_cmpk_eq_i32 s80, 0x880
	s_cselect_b32 s81, s71, s35
	s_cselect_b32 s11, 0x80, s80
	s_cselect_b32 s10, 0, s6
	s_cselect_b32 s6, s51, s7
	s_add_i32 s7, s81, s11
	s_add_i32 s11, s35, s80
	v_add_u32_e32 v252, 0x40000, v250
	v_add_u32_e32 v253, 0x40000, v251
	s_addk_i32 s11, 0xff00
	s_add_i32 s81, s81, s10
	v_add3_u32 v148, v148, v146, 0
	s_mov_b32 m0, s60
	v_add3_u32 v146, v151, v146, 0
	ds_read_b128 v[170:173], v148
	ds_read_b128 v[178:181], v148 offset:2048
	ds_read_b128 v[174:177], v146
	ds_read_b128 v[182:185], v146 offset:2048
	ds_read_b128 v[186:189], v148 offset:4096
	ds_read_b128 v[194:197], v148 offset:6144
	ds_read_b128 v[190:193], v146 offset:4096
	ds_read_b128 v[198:201], v146 offset:6144
	buffer_load_dwordx4 v252, s[88:91], s11 offen lds
	s_mov_b32 m0, s63
	s_nop 0
	buffer_load_dwordx4 v253, s[88:91], s11 offen lds
	s_waitcnt vmcnt(8)
	s_waitcnt lgkmcnt(0)
	s_barrier
	s_setprio 1
	s_waitcnt lgkmcnt(0)
	v_mfma_f32_16x16x128_f8f6f4 v[124:127], v[128:135], v[170:177], v[124:127]
	v_mfma_f32_16x16x128_f8f6f4 v[120:123], v[136:143], v[170:177], v[120:123]
	v_mfma_f32_16x16x128_f8f6f4 v[116:119], v[128:135], v[178:185], v[116:119]
	v_mfma_f32_16x16x128_f8f6f4 v[112:115], v[136:143], v[178:185], v[112:115]
	v_mfma_f32_16x16x128_f8f6f4 v[96:99], v[128:135], v[186:193], v[96:99]
	v_mfma_f32_16x16x128_f8f6f4 v[202:205], v[136:143], v[186:193], v[88:91]
	v_mfma_f32_16x16x128_f8f6f4 v[206:209], v[128:135], v[194:201], v[80:83]
	v_mfma_f32_16x16x128_f8f6f4 v[210:213], v[136:143], v[194:201], v[72:75]
	s_setprio 0
	s_setprio 1
	v_mfma_f32_16x16x128_f8f6f4 v[108:111], v[154:161], v[170:177], v[108:111]
	v_mfma_f32_16x16x128_f8f6f4 v[104:107], v[162:169], v[170:177], v[104:107]
	v_mfma_f32_16x16x128_f8f6f4 v[100:103], v[154:161], v[178:185], v[100:103]
	v_mfma_f32_16x16x128_f8f6f4 v[170:173], v[162:169], v[178:185], v[92:95]
	v_mfma_f32_16x16x128_f8f6f4 v[174:177], v[154:161], v[186:193], v[84:87]
	v_mfma_f32_16x16x128_f8f6f4 v[178:181], v[162:169], v[186:193], v[76:79]
	v_mfma_f32_16x16x128_f8f6f4 v[182:185], v[154:161], v[194:201], v[68:71]
	v_mfma_f32_16x16x128_f8f6f4 v[186:189], v[162:169], v[194:201], v[64:67]
	s_setprio 0
	s_barrier
	s_mov_b32 m0, s43
	s_mov_b32 s10, s90
	s_mov_b32 s11, s91
	s_nop 1
	ds_read_b128 v[64:67], v148 offset:16384
	ds_read_b128 v[72:75], v148 offset:18432
	ds_read_b128 v[68:71], v146 offset:16384
	ds_read_b128 v[76:79], v146 offset:18432
	ds_read_b128 v[80:83], v148 offset:20480
	ds_read_b128 v[88:91], v148 offset:22528
	ds_read_b128 v[84:87], v146 offset:20480
	ds_read_b128 v[92:95], v146 offset:22528
	buffer_load_dwordx4 v144, s[8:11], s6 offen lds
	s_mov_b32 m0, s44
	s_add_i32 s82, s6, 0x40000
	buffer_load_dwordx4 v145, s[8:11], s6 offen lds
	s_mov_b32 m0, s45
	s_nop 0
	buffer_load_dwordx4 v144, s[8:11], s82 offen lds
	s_mov_b32 m0, s46
	s_nop 0
	buffer_load_dwordx4 v145, s[8:11], s82 offen lds
	s_mov_b32 m0, s42
	s_nop 0
	buffer_load_dwordx4 v250, s[88:91], s81 offen lds
	s_mov_b32 m0, s47
	s_nop 0
	buffer_load_dwordx4 v251, s[88:91], s81 offen lds
	s_waitcnt vmcnt(8)
	s_waitcnt lgkmcnt(0)
	s_barrier
	s_setprio 1
	s_waitcnt lgkmcnt(5)
	v_mfma_f32_16x16x128_f8f6f4 v[60:63], v[128:135], v[64:71], v[60:63]
	v_mfma_f32_16x16x128_f8f6f4 v[56:59], v[136:143], v[64:71], v[56:59]
	s_waitcnt lgkmcnt(4)
	v_mfma_f32_16x16x128_f8f6f4 v[48:51], v[128:135], v[72:79], v[48:51]
	v_mfma_f32_16x16x128_f8f6f4 v[190:193], v[136:143], v[72:79], v[40:43]
	s_waitcnt lgkmcnt(1)
	v_mfma_f32_16x16x128_f8f6f4 v[194:197], v[128:135], v[80:87], v[32:35]
	v_mfma_f32_16x16x128_f8f6f4 v[198:201], v[136:143], v[80:87], v[24:27]
	s_waitcnt lgkmcnt(0)
	v_mfma_f32_16x16x128_f8f6f4 v[214:217], v[128:135], v[88:95], v[16:19]
	v_mfma_f32_16x16x128_f8f6f4 v[218:221], v[136:143], v[88:95], v[8:11]
	s_setprio 0
	s_setprio 1
	v_mfma_f32_16x16x128_f8f6f4 v[52:55], v[154:161], v[64:71], v[52:55]
	v_mfma_f32_16x16x128_f8f6f4 v[222:225], v[162:169], v[64:71], v[44:47]
	v_mfma_f32_16x16x128_f8f6f4 v[226:229], v[154:161], v[72:79], v[36:39]
	v_mfma_f32_16x16x128_f8f6f4 v[230:233], v[162:169], v[72:79], v[28:31]
	v_mfma_f32_16x16x128_f8f6f4 v[234:237], v[154:161], v[80:87], v[20:23]
	v_mfma_f32_16x16x128_f8f6f4 v[238:241], v[162:169], v[80:87], v[12:15]
	v_mfma_f32_16x16x128_f8f6f4 v[242:245], v[154:161], v[88:95], v[4:7]
	v_mfma_f32_16x16x128_f8f6f4 v[246:249], v[162:169], v[88:95], v[0:3]
	s_setprio 0
	s_barrier
	s_add_i32 s82, 0, 0x18000
	s_nop 2
	v_add_u32_e32 v4, s82, v150
	v_add_u32_e32 v12, s82, v152
	s_add_i32 s82, 0, 0x1c000
	v_add_u32_e32 v16, s82, v150
	ds_read_b128 v[0:3], v4
	ds_read_b128 v[8:11], v4 offset:2048
	ds_read_b128 v[4:7], v12
	ds_read_b128 v[12:15], v12 offset:2048
	v_add_u32_e32 v17, s82, v152
	ds_read_b128 v[128:131], v16
	ds_read_b128 v[136:139], v16 offset:2048
	ds_read_b128 v[132:135], v17
	ds_read_b128 v[140:143], v17 offset:2048
	s_mov_b32 m0, s48
	ds_read_b128 v[16:19], v148 offset:32768
	ds_read_b128 v[24:27], v148 offset:34816
	ds_read_b128 v[20:23], v146 offset:32768
	ds_read_b128 v[28:31], v146 offset:34816
	ds_read_b128 v[32:35], v148 offset:36864
	ds_read_b128 v[40:43], v148 offset:38912
	ds_read_b128 v[36:39], v146 offset:36864
	ds_read_b128 v[44:47], v146 offset:38912
	buffer_load_dwordx4 v252, s[88:91], s81 offen lds
	s_mov_b32 m0, s49
	s_nop 0
	buffer_load_dwordx4 v253, s[88:91], s81 offen lds
	s_waitcnt vmcnt(8)
	s_waitcnt lgkmcnt(0)
	s_barrier
	s_setprio 1
	s_waitcnt lgkmcnt(5)
	v_mfma_f32_16x16x128_f8f6f4 v[124:127], v[0:7], v[16:23], v[124:127]
	v_mfma_f32_16x16x128_f8f6f4 v[120:123], v[8:15], v[16:23], v[120:123]
	s_waitcnt lgkmcnt(4)
	v_mfma_f32_16x16x128_f8f6f4 v[116:119], v[0:7], v[24:31], v[116:119]
	v_mfma_f32_16x16x128_f8f6f4 v[112:115], v[8:15], v[24:31], v[112:115]
	s_waitcnt lgkmcnt(1)
	v_mfma_f32_16x16x128_f8f6f4 v[96:99], v[0:7], v[32:39], v[96:99]
	v_mfma_f32_16x16x128_f8f6f4 v[88:91], v[8:15], v[32:39], v[202:205]
	s_waitcnt lgkmcnt(0)
	v_mfma_f32_16x16x128_f8f6f4 v[80:83], v[0:7], v[40:47], v[206:209]
	v_mfma_f32_16x16x128_f8f6f4 v[72:75], v[8:15], v[40:47], v[210:213]
	s_setprio 0
	s_setprio 1
	v_mfma_f32_16x16x128_f8f6f4 v[108:111], v[128:135], v[16:23], v[108:111]
	v_mfma_f32_16x16x128_f8f6f4 v[104:107], v[136:143], v[16:23], v[104:107]
	v_mfma_f32_16x16x128_f8f6f4 v[100:103], v[128:135], v[24:31], v[100:103]
	v_mfma_f32_16x16x128_f8f6f4 v[92:95], v[136:143], v[24:31], v[170:173]
	v_mfma_f32_16x16x128_f8f6f4 v[84:87], v[128:135], v[32:39], v[174:177]
	v_mfma_f32_16x16x128_f8f6f4 v[76:79], v[136:143], v[32:39], v[178:181]
	v_mfma_f32_16x16x128_f8f6f4 v[68:71], v[128:135], v[40:47], v[182:185]
	v_mfma_f32_16x16x128_f8f6f4 v[64:67], v[136:143], v[40:47], v[186:189]
	s_setprio 0
	s_barrier
	s_mov_b32 m0, s52
	s_add_i32 s81, s6, 0x80
	ds_read_b128 v[154:157], v148 offset:49152
	ds_read_b128 v[162:165], v148 offset:51200
	ds_read_b128 v[158:161], v146 offset:49152
	ds_read_b128 v[166:169], v146 offset:51200
	ds_read_b128 v[170:173], v148 offset:53248
	ds_read_b128 v[178:181], v148 offset:55296
	ds_read_b128 v[174:177], v146 offset:53248
	ds_read_b128 v[182:185], v146 offset:55296
	buffer_load_dwordx4 v144, s[8:11], s81 offen lds
	s_mov_b32 m0, s53
	s_add_i32 s6, s6, 0x40080
	buffer_load_dwordx4 v145, s[8:11], s81 offen lds
	s_mov_b32 m0, s56
	s_nop 0
	buffer_load_dwordx4 v144, s[8:11], s6 offen lds
	s_mov_b32 m0, s57
	s_nop 0
	buffer_load_dwordx4 v145, s[8:11], s6 offen lds
	s_mov_b32 m0, s54
	s_nop 0
	buffer_load_dwordx4 v250, s[88:91], s7 offen lds
	s_mov_b32 m0, s55
	s_nop 0
	buffer_load_dwordx4 v251, s[88:91], s7 offen lds
	s_waitcnt vmcnt(8)
	s_waitcnt lgkmcnt(0)
	s_barrier
	s_setprio 1
	s_waitcnt lgkmcnt(5)
	v_mfma_f32_16x16x128_f8f6f4 v[60:63], v[0:7], v[154:161], v[60:63]
	v_mfma_f32_16x16x128_f8f6f4 v[56:59], v[8:15], v[154:161], v[56:59]
	s_waitcnt lgkmcnt(4)
	v_mfma_f32_16x16x128_f8f6f4 v[48:51], v[0:7], v[162:169], v[48:51]
	v_mfma_f32_16x16x128_f8f6f4 v[40:43], v[8:15], v[162:169], v[190:193]
	s_waitcnt lgkmcnt(1)
	v_mfma_f32_16x16x128_f8f6f4 v[32:35], v[0:7], v[170:177], v[194:197]
	v_mfma_f32_16x16x128_f8f6f4 v[24:27], v[8:15], v[170:177], v[198:201]
	s_waitcnt lgkmcnt(0)
	v_mfma_f32_16x16x128_f8f6f4 v[16:19], v[0:7], v[178:185], v[214:217]
	v_mfma_f32_16x16x128_f8f6f4 v[8:11], v[8:15], v[178:185], v[218:221]
	s_setprio 0
	s_setprio 1
	v_mfma_f32_16x16x128_f8f6f4 v[52:55], v[128:135], v[154:161], v[52:55]
	v_mfma_f32_16x16x128_f8f6f4 v[44:47], v[136:143], v[154:161], v[222:225]
	v_mfma_f32_16x16x128_f8f6f4 v[36:39], v[128:135], v[162:169], v[226:229]
	v_mfma_f32_16x16x128_f8f6f4 v[28:31], v[136:143], v[162:169], v[230:233]
	v_mfma_f32_16x16x128_f8f6f4 v[20:23], v[128:135], v[170:177], v[234:237]
	v_mfma_f32_16x16x128_f8f6f4 v[12:15], v[136:143], v[170:177], v[238:241]
	v_mfma_f32_16x16x128_f8f6f4 v[4:7], v[128:135], v[178:185], v[242:245]
	v_mfma_f32_16x16x128_f8f6f4 v[0:3], v[136:143], v[178:185], v[246:249]
	s_setprio 0
	s_barrier
	s_add_i32 s79, s79, 2
	s_addk_i32 s80, 0x100
	s_cmp_gt_u32 s79, 13
	s_cbranch_scc1 .LBB0_2574
